# speedup vs baseline: 1.0041x; 1.0041x over previous
_Z16rec_chunk_kernelPKDF16_PKfS2_S2_PfS3_:
	s_load_dwordx4 s[12:15], s[0:1], 0x0
	s_cmpk_lt_u32 s2, 0xc0
	s_mov_b64 s[4:5], -1
	s_cbranch_scc0 .LBB2_4
	s_load_dwordx8 s[4:11], s[0:1], 0x10
	s_bfe_u32 s1, s2, 0x80003
	s_mulk_i32 s1, 0xab
	s_lshr_b32 s1, s1, 10
	s_lshr_b32 s0, s2, 3
	s_mul_i32 s1, s1, 6
	s_sub_i32 s0, s0, s1
	s_and_b32 s22, s0, 0xff
	s_lshl_b32 s0, s2, 2
	s_and_b32 s23, s0, 28
	s_and_b32 s0, s2, 0xff
	s_mulk_i32 s0, 0xab
	s_lshr_b32 s33, s0, 13
	s_add_i32 s23, s23, s33
	s_mov_b32 s19, 0x20000
	s_mov_b32 s18, 0xa80000
	s_waitcnt lgkmcnt(0)
	s_and_b32 s17, s13, 0xffff
	s_mul_i32 s3, s23, 0x54000
	s_mov_b32 s28, s12
	s_mov_b32 s29, s17
	s_mov_b32 s30, s18
	s_mov_b32 s31, s19
	v_lshlrev_b32_e32 v1, 4, v0
	s_or_b32 s1, s3, 0x1800
	s_and_b32 s21, s9, 0xffff
	buffer_load_dwordx4 v[162:165], v1, s[28:31], s3 offen
	buffer_load_dwordx4 v[158:161], v1, s[28:31], s1 offen
	s_or_b32 s1, s3, 0x3000
	s_add_i32 s9, s3, 0x4800
	buffer_load_dwordx4 v[154:157], v1, s[28:31], s1 offen
	buffer_load_dwordx4 v[178:181], v1, s[28:31], s9 offen
	s_or_b32 s1, s3, 0x400
	s_or_b32 s9, s3, 0x1c00
	buffer_load_dwordx4 v[186:189], v1, s[28:31], s1 offen
	buffer_load_dwordx4 v[190:193], v1, s[28:31], s9 offen
	s_or_b32 s1, s3, 0x3400
	s_add_i32 s9, s3, 0x4c00
	buffer_load_dwordx4 v[194:197], v1, s[28:31], s1 offen
	buffer_load_dwordx4 v[182:185], v1, s[28:31], s9 offen
	s_or_b32 s1, s3, 0x800
	s_or_b32 s9, s3, 0x2000
	buffer_load_dwordx4 v[150:153], v1, s[28:31], s1 offen
	buffer_load_dwordx4 v[138:141], v1, s[28:31], s9 offen
	s_or_b32 s1, s3, 0x3800
	s_add_i32 s9, s3, 0x5000
	buffer_load_dwordx4 v[146:149], v1, s[28:31], s1 offen
	buffer_load_dwordx4 v[134:137], v1, s[28:31], s9 offen
	s_or_b32 s1, s3, 0xc00
	s_or_b32 s9, s3, 0x2400
	buffer_load_dwordx4 v[142:145], v1, s[28:31], s1 offen
	buffer_load_dwordx4 v[170:173], v1, s[28:31], s9 offen
	s_or_b32 s1, s3, 0x3c00
	s_add_i32 s9, s3, 0x5400
	s_mul_i32 s0, s23, 48
	buffer_load_dwordx4 v[174:177], v1, s[28:31], s1 offen
	buffer_load_dwordx4 v[166:169], v1, s[28:31], s9 offen
	s_or_b32 s1, s3, 0x1000
	s_or_b32 s9, s3, 0x2800
	s_or_b32 s0, s0, s22
	buffer_load_dwordx4 v[122:125], v1, s[28:31], s1 offen
	buffer_load_dwordx4 v[130:133], v1, s[28:31], s9 offen
	s_add_i32 s1, s3, 0x4000
	s_add_i32 s9, s3, 0x5800
	s_mov_b32 s26, 0xc00000
	buffer_load_dwordx4 v[126:129], v1, s[28:31], s1 offen
	buffer_load_dwordx4 v[114:117], v1, s[28:31], s9 offen
	s_or_b32 s1, s3, 0x1400
	s_and_b32 s25, s15, 0xffff
	s_lshl_b32 s9, s0, 13
	buffer_load_dwordx4 v[118:121], v1, s[28:31], s1 offen
	s_mov_b32 s28, s14
	s_mov_b32 s29, s25
	s_mov_b32 s30, s26
	s_or_b32 s0, s9, 0x400
	buffer_load_dwordx4 v[50:53], v1, s[28:31], s9 offen
	buffer_load_dwordx4 v[54:57], v1, s[28:31], s0 offen
	s_or_b32 s0, s9, 0x800
	s_or_b32 s35, s9, 0xc00
	buffer_load_dwordx4 v[58:61], v1, s[28:31], s0 offen
	buffer_load_dwordx4 v[62:65], v1, s[28:31], s35 offen
	s_or_b32 s0, s9, 0x1000
	s_lshr_b32 s1, s23, 3
	s_or_b32 s35, s9, 0x1400
	buffer_load_dwordx4 v[66:69], v1, s[28:31], s0 offen
	buffer_load_dwordx4 v[70:73], v1, s[28:31], s35 offen
	s_or_b32 s0, s9, 0x1800
	s_or_b32 s35, s9, 0x1c00
	buffer_load_dwordx4 v[74:77], v1, s[28:31], s0 offen
	buffer_load_dwordx4 v[78:81], v1, s[28:31], s35 offen
	s_mul_i32 s0, s23, 0x4800
	s_mulk_i32 s1, 0x3000
	s_add_i32 s1, s1, s0
	v_lshrrev_b32_e32 v2, 3, v0
	s_lshl_b32 s0, s22, 7
	s_lshl_b32 s1, s1, 2
	v_and_b32_e32 v2, 4, v2
	s_or_b32 s28, s1, s0
	v_mul_u32_u24_e32 v2, 0xc0, v2
	s_add_u32 s0, s6, s28
	v_and_or_b32 v2, v0, 31, v2
	s_addc_u32 s1, s7, 0
	v_lshlrev_b32_e32 v226, 2, v2
	v_mov_b32_e32 v227, 0
	s_movk_i32 s27, 0x1000
	v_lshl_add_u64 v[30:31], s[0:1], 0, v[226:227]
	v_add_co_u32_e32 v2, vcc, s27, v30
	s_movk_i32 s20, 0x2000
	s_nop 0
	v_addc_co_u32_e32 v3, vcc, 0, v31, vcc
	v_add_co_u32_e32 v4, vcc, s20, v30
	s_movk_i32 s16, 0x3000
	s_nop 0
	v_addc_co_u32_e32 v5, vcc, 0, v31, vcc
	v_add_co_u32_e32 v6, vcc, s16, v30
	s_movk_i32 s34, 0x4000
	s_nop 0
	v_addc_co_u32_e32 v7, vcc, 0, v31, vcc
	global_load_dword v38, v[2:3], off offset:2048 nt
	global_load_dword v39, v[2:3], off offset:2816 nt
	global_load_dword v40, v[2:3], off offset:3584 nt
	global_load_dword v41, v[4:5], off offset:256 nt
	global_load_dword v42, v[6:7], off nt
	global_load_dword v43, v[6:7], off offset:768 nt
	global_load_dword v44, v[6:7], off offset:1536 nt
	global_load_dword v45, v[6:7], off offset:2304 nt
	v_add_co_u32_e32 v2, vcc, s34, v30
	s_movk_i32 s24, 0x5000
	s_nop 0
	v_addc_co_u32_e32 v3, vcc, 0, v31, vcc
	v_add_co_u32_e32 v4, vcc, s24, v30
	s_movk_i32 s6, 0x6000
	s_nop 0
	v_addc_co_u32_e32 v5, vcc, 0, v31, vcc
	v_add_co_u32_e32 v6, vcc, s6, v30
	s_movk_i32 s6, 0x7000
	s_nop 0
	v_addc_co_u32_e32 v7, vcc, 0, v31, vcc
	v_add_co_u32_e32 v8, vcc, s6, v30
	s_mov_b32 s6, 0x8000
	s_nop 0
	v_addc_co_u32_e32 v9, vcc, 0, v31, vcc
	v_add_co_u32_e32 v10, vcc, s6, v30
	s_mov_b32 s6, 0x9000
	s_nop 0
	v_addc_co_u32_e32 v11, vcc, 0, v31, vcc
	v_add_co_u32_e32 v14, vcc, s6, v30
	s_mov_b32 s6, 0xa000
	s_nop 0
	v_addc_co_u32_e32 v15, vcc, 0, v31, vcc
	v_add_co_u32_e32 v16, vcc, s6, v30
	s_mov_b32 s6, 0xb000
	s_nop 0
	v_addc_co_u32_e32 v17, vcc, 0, v31, vcc
	v_add_co_u32_e32 v18, vcc, s6, v30
	s_mov_b32 s6, 0xc000
	s_nop 0
	v_addc_co_u32_e32 v19, vcc, 0, v31, vcc
	v_add_co_u32_e32 v22, vcc, s6, v30
	s_mov_b32 s6, 0xd000
	s_nop 0
	v_addc_co_u32_e32 v23, vcc, 0, v31, vcc
	v_add_co_u32_e32 v24, vcc, s6, v30
	s_mov_b32 s6, 0xe000
	s_nop 0
	v_addc_co_u32_e32 v25, vcc, 0, v31, vcc
	v_add_co_u32_e32 v26, vcc, s6, v30
	s_mov_b32 s6, 0xf000
	s_nop 0
	v_addc_co_u32_e32 v27, vcc, 0, v31, vcc
	v_add_co_u32_e32 v32, vcc, s6, v30
	s_mov_b32 s6, 0x10000
	s_nop 0
	v_addc_co_u32_e32 v33, vcc, 0, v31, vcc
	global_load_dword v46, v[2:3], off offset:2048 nt
	global_load_dword v47, v[2:3], off offset:2816 nt
	global_load_dword v48, v[2:3], off offset:3584 nt
	global_load_dword v49, v[4:5], off offset:256 nt
	s_nop 0
	global_load_dword v2, v[6:7], off nt
	global_load_dword v3, v[6:7], off offset:768 nt
	global_load_dword v4, v[6:7], off offset:1536 nt
	global_load_dword v5, v[6:7], off offset:2304 nt
	s_nop 0
	global_load_dword v6, v[8:9], off offset:2048 nt
	global_load_dword v7, v[8:9], off offset:2816 nt
	s_nop 0
	global_load_dword v8, v[8:9], off offset:3584 nt
	s_nop 0
	global_load_dword v9, v[10:11], off offset:256 nt
	s_nop 0
	global_load_dword v10, v[14:15], off nt
	global_load_dword v11, v[14:15], off offset:768 nt
	global_load_dword v12, v[14:15], off offset:1536 nt
	global_load_dword v13, v[14:15], off offset:2304 nt
	s_nop 0
	global_load_dword v14, v[16:17], off offset:2048 nt
	global_load_dword v15, v[16:17], off offset:2816 nt
	s_nop 0
	global_load_dword v16, v[16:17], off offset:3584 nt
	s_nop 0
	global_load_dword v17, v[18:19], off offset:256 nt
	s_nop 0
	global_load_dword v18, v[22:23], off nt
	global_load_dword v19, v[22:23], off offset:768 nt
	global_load_dword v20, v[22:23], off offset:1536 nt
	global_load_dword v21, v[22:23], off offset:2304 nt
	s_nop 0
	global_load_dword v22, v[24:25], off offset:2048 nt
	global_load_dword v23, v[24:25], off offset:2816 nt
	s_nop 0
	global_load_dword v24, v[24:25], off offset:3584 nt
	s_nop 0
	global_load_dword v25, v[26:27], off offset:256 nt
	s_nop 0
	global_load_dword v26, v[32:33], off nt
	global_load_dword v27, v[32:33], off offset:768 nt
	global_load_dword v28, v[32:33], off offset:1536 nt
	global_load_dword v29, v[32:33], off offset:2304 nt
	v_add_co_u32_e32 v32, vcc, s6, v30
	s_mov_b32 s6, 0x11000
	s_nop 0
	v_addc_co_u32_e32 v33, vcc, 0, v31, vcc
	v_add_co_u32_e32 v82, vcc, s6, v30
	s_mov_b32 s16, s12
	s_nop 0
	v_addc_co_u32_e32 v83, vcc, 0, v31, vcc
	global_load_dword v34, v226, s[0:1] nt
	global_load_dword v35, v226, s[0:1] offset:768 nt
	global_load_dword v36, v226, s[0:1] offset:1536 nt
	global_load_dword v37, v226, s[0:1] offset:2304 nt
	global_load_dword v30, v[32:33], off offset:2048 nt
	global_load_dword v31, v[32:33], off offset:2816 nt
	s_nop 0
	global_load_dword v32, v[32:33], off offset:3584 nt
	s_nop 0
	global_load_dword v33, v[82:83], off offset:256 nt
	s_mov_b32 s20, s8
	s_mov_b32 s27, s19
	s_mov_b32 s24, s14
	s_mov_b32 s6, 0
	s_and_b32 s0, s2, 7
	s_mulk_i32 s0, 0xc0
	s_mul_i32 s33, s33, 48
	s_add_i32 s0, s0, s33
	s_or_b32 s0, s0, s22
	s_lshl_b32 s0, s0, 13
	s_or_b32 s7, s0, 0x1c00
	s_lshl_b32 s0, s23, 5
	s_add_u32 s0, s4, s0
	s_addc_u32 s1, s5, 0
	s_mov_b32 s4, 1
